# s12
# baseline (speedup 1.0000x reference)
_Z11prep_kernelPKfS0_PKiS2_S0_S0_S0_S0_S0_S0_Pc:
	s_lshr_b32 s4, s2, 2
	v_lshrrev_b32_e32 v2, 6, v0
	s_and_b32 s4, s4, 0x1ffffffe
	s_load_dwordx4 s[28:31], s[0:1], 0x40
	s_load_dwordx8 s[12:19], s[0:1], 0x0
	s_load_dwordx8 s[20:27], s[0:1], 0x20
	s_load_dwordx2 s[32:33], s[0:1], 0x50
	v_and_b32_e32 v1, 15, v0
	s_and_b32 s3, s2, 7
	v_or_b32_e32 v2, s4, v2
	v_lshl_or_b32 v88, v2, 3, s3
	v_cmp_gt_u32_e64 s[10:11], 14, v1
	v_mul_lo_u32 v7, v88, 14
	v_and_b32_e32 v105, 63, v0
	v_cndmask_b32_e64 v6, 13, v1, s[10:11]
	v_add_u32_e32 v2, v7, v6
	v_mul_u32_u24_e32 v4, 12, v2
	v_lshlrev_b32_e32 v5, 2, v6
	v_cmp_gt_u32_e64 s[8:9], 48, v105
	v_cmp_gt_u32_e64 s[6:7], 14, v105
	v_lshlrev_b32_e32 v118, 1, v0
	v_lshrrev_b32_e32 v104, 4, v0
	v_cndmask_b32_e64 v8, 0, v105, s[8:9]
	v_cndmask_b32_e64 v9, 0, v105, s[6:7]
	v_mad_u32_u24 v8, v88, 48, v8
	v_add_lshl_u32 v9, v7, v9, 2
	v_lshlrev_b32_e32 v8, 2, v8
	s_lshl_b32 s2, s2, 3
	s_and_b32 s2, s2, 0x78
	v_and_b32_e32 v106, 30, v118
	v_or_b32_e32 v107, s2, v104
	v_cmp_gt_u32_e64 s[2:3], 23, v106
	v_or_b32_e32 v10, 1, v106
	v_cmp_gt_u32_e64 s[4:5], 23, v10
	v_lshlrev_b32_e32 v11, 7, v106
	v_lshlrev_b32_e32 v10, 7, v10
	v_cndmask_b32_e64 v11, 0, v11, s[2:3]
	v_cndmask_b32_e64 v10, 0, v10, s[4:5]
	v_or_b32_e32 v11, v11, v107
	v_or_b32_e32 v10, v10, v107
	v_lshlrev_b32_e32 v11, 2, v11
	v_lshlrev_b32_e32 v10, 2, v10
	v_lshlrev_b32_e32 v12, 2, v107
	v_lshlrev_b32_e32 v119, 5, v0
	v_lshlrev_b32_e32 v13, 2, v0
	v_and_b32_e32 v109, 12, v13
	v_and_b32_e32 v91, 0xf80, v119
	v_lshl_or_b32 v91, v109, 2, v91
	v_or_b32_e32 v92, 0x1000, v91
	v_lshlrev_b32_e32 v90, 9, v2
	v_and_b32_e32 v16, 48, v0
	v_or_b32_e32 v90, v90, v16
	v_or_b32_e32 v112, 0x80, v0
	v_or_b32_e32 v111, 0x180, v0
	v_or_b32_e32 v108, 0x280, v0
	v_mov_b32_e32 v87, 0
	v_bfe_u32 v110, v0, 4, 2
	s_movk_i32 s34, 0x60
	v_lshrrev_b32_e32 v136, 1, v0
	v_lshrrev_b32_e32 v18, 3, v0
	v_and_b32_e32 v18, 4, v18
	v_and_b32_e32 v19, 24, v0
	v_and_b32_e32 v20, 2, v136
	v_or3_b32 v18, v18, v19, v20
	v_and_or_b32 v136, v136, s34, v18
	v_mul_u32_u24_e32 v18, 0x110, v109
	v_lshl_add_u32 v136, v136, 1, v18
	v_add_u32_e32 v137, 0x1100, v136
	v_add_u32_e32 v138, 0x2200, v136
	v_lshlrev_b32_e32 v18, 9, v88
	v_and_b32_e32 v19, 0x100, v119
	v_lshlrev_b32_e32 v20, 4, v0
	v_and_b32_e32 v20, 48, v20
	v_or3_b32 v139, v18, v19, v20
	v_and_b32_e32 v19, 8, v118
	v_and_b32_e32 v20, 64, v118
	v_or3_b32 v139, v139, v19, v20
	v_lshlrev_b32_e32 v19, 2, v110
	v_and_b32_e32 v20, 4, v19
	v_or_b32_e32 v139, v139, v20
	v_lshl_or_b32 v140, v1, 5, v18
	v_or_b32_e32 v140, v140, v19
	v_add_u32_e32 v140, 0x80000, v140
	v_lshl_or_b32 v141, v88, 4, v1
	v_lshlrev_b32_e32 v141, 3, v141
	v_add_u32_e32 v141, 0x140000, v141
	v_lshlrev_b32_e32 v20, 8, v88
	v_mul_u32_u24_e32 v21, 43, v105
	v_lshrrev_b32_e32 v21, 9, v21
	v_mul_u32_u24_e32 v21, 12, v21
	v_sub_u32_e32 v22, v105, v21
	v_and_b32_e32 v142, 3, v22
	v_lshrrev_b32_e32 v22, 2, v22
	v_mad_u32_u24 v142, v142, 3, v22
	v_add_u32_e32 v142, v142, v21
	v_lshl_add_u32 v142, v142, 2, v20
	v_add_u32_e32 v142, 0x164000, v142
	v_lshl_add_u32 v143, v105, 2, v20
	v_add_u32_e32 v143, 0x164000, v143
	v_lshlrev_b32_e32 v123, 6, v107
	v_lshl_add_u32 v123, v106, 1, v123
	v_add_u32_e32 v123, 0x160000, v123
	v_lshl_add_u32 v122, v1, 4, v20
	v_or_b32_e32 v122, v122, v19
	v_add_u32_e32 v122, 0x100000, v122
	s_waitcnt lgkmcnt(0)
	global_load_dwordx3 v[82:84], v4, s[12:13]
	global_load_dword v85, v5, s[26:27]
	global_load_dword v114, v8, s[18:19]
	global_load_dword v115, v9, s[16:17]
	global_load_dword v116, v11, s[28:29]
	global_load_dword v113, v10, s[28:29]
	global_load_dword v117, v12, s[30:31]
	global_load_dwordx4 v[66:69], v91, s[20:21]
	global_load_dwordx4 v[70:73], v91, s[20:21] offset:64
	global_load_dwordx4 v[74:77], v92, s[20:21]
	global_load_dwordx4 v[78:81], v92, s[20:21] offset:64
	global_load_dwordx4 v[58:61], v91, s[22:23]
	global_load_dwordx4 v[62:65], v91, s[22:23] offset:64
	global_load_dwordx4 v[50:53], v92, s[22:23]
	global_load_dwordx4 v[54:57], v92, s[22:23] offset:64
	global_load_dwordx4 v[42:45], v91, s[24:25]
	global_load_dwordx4 v[46:49], v91, s[24:25] offset:64
	global_load_dwordx4 v[34:37], v92, s[24:25]
	global_load_dwordx4 v[38:41], v92, s[24:25] offset:64
	global_load_dwordx4 v[26:29], v90, s[14:15] nt
	global_load_dwordx4 v[30:33], v90, s[14:15] offset:64 nt
	global_load_dwordx4 v[18:21], v90, s[14:15] offset:128 nt
	global_load_dwordx4 v[22:25], v90, s[14:15] offset:192 nt
	global_load_dwordx4 v[10:13], v90, s[14:15] offset:256 nt
	global_load_dwordx4 v[14:17], v90, s[14:15] offset:320 nt
	global_load_dwordx4 v[2:5], v90, s[14:15] offset:384 nt
	global_load_dwordx4 v[6:9], v90, s[14:15] offset:448 nt
	s_waitcnt vmcnt(26)
	v_mov_b32_e32 v90, v83
	v_mov_b32_e32 v91, v84
	v_lshlrev_b32_e32 v86, 2, v110
	s_waitcnt vmcnt(25)
	v_mul_f32_e32 v84, 0x3fb8aa3b, v85
	s_mov_b32 s14, 0x41700000
	v_exp_f32_e32 v84, v84
	v_cndmask_b32_e64 v94, 0, 1.0, s[10:11]
	v_add_f32_e32 v84, 1.0, v84
	v_cmp_lt_f32_e32 vcc, s14, v85
	v_log_f32_e32 v84, v84
	v_cmp_lt_u32_e64 s[12:13], 15, v105
	v_mul_f32_e32 v84, 0x3f317218, v84
	v_cndmask_b32_e32 v84, v84, v85, vcc
	v_mul_f32_e32 v84, 0xbe715bef, v84
	v_mul_f32_e32 v84, 0x3f3504f3, v84
	v_mul_f32_e32 v84, 0x41800000, v84
	v_cndmask_b32_e64 v99, 0, v84, s[10:11]
	v_mul_f32_e32 v101, -2.0, v99
	v_mov_b32_e32 v95, v101
	v_pk_mul_f32 v[84:85], v[94:95], v[82:83] op_sel:[0,1]
	v_cmp_gt_u32_e32 vcc, 16, v105
	v_mov_b32_e32 v83, v85
	s_and_saveexec_b64 s[14:15], s[12:13]
	s_xor_b64 s[14:15], exec, s[14:15]
	s_cbranch_execz .LBB0_10
	v_pk_mul_f32 v[92:93], v[90:91], v[90:91]
	v_mov_b32_e32 v95, v91
	v_fma_f32 v83, v82, v82, v92
	v_add_f32_e32 v100, v83, v93
	v_pk_mul_f32 v[92:93], v[94:95], v[100:101]
	v_mov_b32_e32 v83, v87
	v_cvt_pk_fp8_f32 v83, v93, 0
	v_mul_f32_e32 v98, v94, v91
	v_cmp_lt_i32_e64 s[12:13], 1, v110
	s_mov_b64 s[16:17], 0
	v_cvt_f32_fp8_e32 v83, v83
	v_sub_f32_e32 v89, v93, v83
	s_and_saveexec_b64 s[18:19], s[12:13]
	s_xor_b64 s[18:19], exec, s[18:19]
	s_cbranch_execz .LBB0_5
	v_cmp_eq_u32_e64 s[12:13], 2, v110
	s_mov_b64 s[20:21], -1
	s_and_saveexec_b64 s[16:17], s[12:13]
	s_cbranch_execz .LBB0_4
	v_mov_b32_e32 v83, 0
	v_mov_b32_e32 v84, 0
	v_mov_b32_e32 v89, 0
	v_cvt_pk_fp8_f32 v84, v99, 0
	v_cvt_pk_fp8_f32 v89, v98, 0
	v_cvt_pk_fp8_f32 v83, v92, 0
	s_xor_b64 s[20:21], exec, -1
	v_cvt_f32_fp8_e32 v85, v84
	v_cvt_f32_fp8_e32 v84, v89
	v_cvt_f32_fp8_e32 v83, v83
	v_mov_b32_e32 v102, v92
	v_pk_add_f32 v[96:97], v[98:99], v[84:85] neg_lo:[0,1] neg_hi:[0,1]
	v_sub_f32_e32 v84, v92, v83

.LBB0_10:
	s_or_saveexec_b64 s[14:15], s[14:15]
	s_xor_b64 exec, exec, s[14:15]
	s_cbranch_execz .LBB0_12
	v_pk_mul_f32 v[92:93], v[94:95], v[82:83] op_sel_hi:[1,0]
	v_mov_b32_e32 v85, 0
	v_mov_b32_e32 v89, 0
	v_cvt_pk_fp8_f32 v89, v92, 0
	v_cvt_pk_fp8_f32 v85, v93, 0
	v_mov_b32_e32 v96, v92
	v_mov_b32_e32 v97, v93
	v_cvt_f32_fp8_e32 v98, v89
	v_cvt_f32_fp8_e32 v99, v85
	v_pk_fma_f32 v[102:103], v[94:95], v[82:83], v[98:99] op_sel_hi:[1,0,1] neg_lo:[0,0,1] neg_hi:[0,0,1]
.LBB0_12:
	s_or_b64 exec, exec, s[14:15]
	v_cvt_pk_fp8_f32 v119, v93, v103
	s_nop 0
	v_cvt_pk_fp8_f32 v103, v96, v92
	v_cvt_pk_fp8_f32 v119, v97, v83 op_sel:[0,0,1]
	v_cvt_pk_fp8_f32 v103, v102, v84 op_sel:[0,0,1]
	s_nop 0
	global_store_dword v139, v119, s[32:33] offset:128
	global_store_dword v140, v103, s[32:33] offset:16
	s_and_saveexec_b64 s[0:1], vcc
	s_cbranch_execz .LBB0_14
	v_cvt_f16_f32_e32 v83, v82
	v_cvt_pk_f16_f32 v90, v90, v91
	s_nop 0
	v_alignbit_b32 v91, 0, v90, 16
	v_pack_b32_f16 v90, v83, v90
	global_store_dwordx2 v141, v[90:91], s[32:33]
.LBB0_14:
	s_or_b64 exec, exec, s[0:1]
	s_and_saveexec_b64 s[0:1], s[8:9]
	s_cbranch_execz .LBB0_16
	s_waitcnt vmcnt(26)
	global_store_dword v142, v114, s[32:33]
.LBB0_16:
	s_or_b64 exec, exec, s[0:1]
	s_waitcnt vmcnt(25)
	v_cmp_ne_u32_e32 vcc, 0, v115
	s_and_b64 s[0:1], s[6:7], vcc
	v_cndmask_b32_e64 v91, 0, 1, s[0:1]
	v_cmp_gt_u32_e64 s[0:1], 2, v105
	s_nop 0
	v_cmp_ne_u32_e32 vcc, 0, v91
	s_and_saveexec_b64 s[6:7], s[0:1]
	s_cbranch_execz .LBB0_18
	s_and_b32 s0, vcc_lo, 0x3fff
	v_mov_b32_e32 v90, s0
	global_store_dword v143, v90, s[32:33] offset:192
.LBB0_18:
	s_or_b64 exec, exec, s[6:7]
	s_waitcnt vmcnt(22)
	v_cmp_eq_u32_e32 vcc, 22, v106
	v_cvt_f16_f32_e32 v89, v117
	v_cvt_f16_f32_e32 v88, v116
	v_cvt_f16_f32_e32 v90, v113
	v_cndmask_b32_e64 v88, 0, v88, s[2:3]
	v_cndmask_b32_e32 v89, 0, v89, vcc
	v_cndmask_b32_e64 v89, v89, v90, s[4:5]
	v_pack_b32_f16 v96, v88, v89
	global_store_dword v123, v96, s[32:33]
	s_waitcnt vmcnt(21)
	v_cvt_pk_f16_f32 v66, v66, v70
	v_cvt_pk_f16_f32 v67, v67, v71
	v_cvt_pk_f16_f32 v68, v68, v72
	v_cvt_pk_f16_f32 v69, v69, v73
	ds_write2_b32 v136, v66, v67 offset0:0 offset1:68
	ds_write2_b32 v136, v68, v69 offset0:136 offset1:204
	s_waitcnt vmcnt(19)
	v_cvt_pk_f16_f32 v74, v74, v78
	v_cvt_pk_f16_f32 v75, v75, v79
	v_cvt_pk_f16_f32 v76, v76, v80
	v_cvt_pk_f16_f32 v77, v77, v81
	ds_write2_b32 v136, v74, v75 offset0:32 offset1:100
	ds_write2_b32 v136, v76, v77 offset0:168 offset1:236
	s_waitcnt vmcnt(17)
	v_cvt_pk_f16_f32 v58, v58, v62
	v_cvt_pk_f16_f32 v59, v59, v63
	v_cvt_pk_f16_f32 v60, v60, v64
	v_cvt_pk_f16_f32 v61, v61, v65
	ds_write2_b32 v137, v58, v59 offset0:0 offset1:68
	ds_write2_b32 v137, v60, v61 offset0:136 offset1:204
	s_waitcnt vmcnt(15)
	v_cvt_pk_f16_f32 v50, v50, v54
	v_cvt_pk_f16_f32 v51, v51, v55
	v_cvt_pk_f16_f32 v52, v52, v56
	v_cvt_pk_f16_f32 v53, v53, v57
	ds_write2_b32 v137, v50, v51 offset0:32 offset1:100
	ds_write2_b32 v137, v52, v53 offset0:168 offset1:236
	s_waitcnt vmcnt(13)
	v_cvt_pk_f16_f32 v42, v42, v46
	v_cvt_pk_f16_f32 v43, v43, v47
	v_cvt_pk_f16_f32 v44, v44, v48
	v_cvt_pk_f16_f32 v45, v45, v49
	ds_write2_b32 v138, v42, v43 offset0:0 offset1:68
	ds_write2_b32 v138, v44, v45 offset0:136 offset1:204
	s_waitcnt vmcnt(11)
	v_cvt_pk_f16_f32 v34, v34, v38
	v_cvt_pk_f16_f32 v35, v35, v39
	v_cvt_pk_f16_f32 v36, v36, v40
	v_cvt_pk_f16_f32 v37, v37, v41
	ds_write2_b32 v138, v34, v35 offset0:32 offset1:100
	ds_write2_b32 v138, v36, v37 offset0:168 offset1:236
	s_movk_i32 s0, 0x110
	s_waitcnt vmcnt(9)
	v_cvt_pk_f16_f32 v39, v32, v33
	v_lshlrev_b32_e32 v32, 4, v110
	v_mad_u32_u24 v48, v1, s0, v32
	s_waitcnt lgkmcnt(0)
	s_barrier
	ds_read_b128 v[32:35], v48
	v_cvt_pk_f16_f32 v38, v30, v31
	v_cvt_pk_f16_f32 v37, v28, v29
	v_cvt_pk_f16_f32 v36, v26, v27
	ds_read_b128 v[26:29], v48 offset:64
	s_waitcnt vmcnt(7)
	v_cvt_pk_f16_f32 v25, v24, v25
	s_waitcnt lgkmcnt(1)
	v_mfma_f32_16x16x32_f16 v[124:127], v[32:35], v[36:39], 0
	ds_read_b128 v[30:33], v48 offset:4352
	ds_read_b128 v[40:43], v48 offset:4416
	v_cvt_pk_f16_f32 v24, v22, v23
	s_waitcnt lgkmcnt(1)
	v_mfma_f32_16x16x32_f16 v[128:131], v[30:33], v[36:39], 0
	ds_read_b128 v[30:33], v48 offset:8704
	ds_read_b128 v[44:47], v48 offset:8768
	v_cvt_pk_f16_f32 v23, v20, v21
	v_cvt_pk_f16_f32 v22, v18, v19
	s_waitcnt lgkmcnt(1)
	v_mfma_f32_16x16x32_f16 v[132:135], v[36:39], v[30:33], 0
	s_waitcnt vmcnt(5)
	v_cvt_pk_f16_f32 v0, v16, v17
	ds_read_b128 v[16:19], v48 offset:128
	v_lshlrev_b32_e32 v88, 4, v1
	v_mfma_f32_16x16x32_f16 v[124:127], v[26:29], v[22:25], v[124:127]
	v_mfma_f32_16x16x32_f16 v[128:131], v[40:43], v[22:25], v[128:131]
	s_waitcnt lgkmcnt(1)
	v_mfma_f32_16x16x32_f16 v[132:135], v[22:25], v[44:47], v[132:135]
	v_cndmask_b32_e64 v23, 0, v0, s[10:11]
	v_cvt_pk_f16_f32 v22, v14, v15
	v_cvt_pk_f16_f32 v21, v12, v13
	v_cvt_pk_f16_f32 v20, v10, v11
	ds_read_b128 v[10:13], v48 offset:192
	s_waitcnt vmcnt(3)
	v_cvt_pk_f16_f32 v9, v8, v9
	s_waitcnt lgkmcnt(1)
	v_mfma_f32_16x16x32_f16 v[124:127], v[16:19], v[20:23], v[124:127]
	v_cvt_pk_f16_f32 v8, v6, v7
	v_cvt_pk_f16_f32 v7, v4, v5
	ds_read_b128 v[14:17], v48 offset:4480
	ds_read_b128 v[24:27], v48 offset:4544
	v_cvt_pk_f16_f32 v6, v2, v3
	s_waitcnt lgkmcnt(1)
	v_mfma_f32_16x16x32_f16 v[128:131], v[14:17], v[20:23], v[128:131]
	ds_read_b128 v[14:17], v48 offset:8832
	ds_read_b128 v[28:31], v48 offset:8896
	v_mfma_f32_16x16x32_f16 v[124:127], v[10:13], v[6:9], v[124:127]
	s_waitcnt lgkmcnt(2)
	v_mfma_f32_16x16x32_f16 v[128:131], v[24:27], v[6:9], v[128:131]
	s_waitcnt lgkmcnt(1)
	v_mfma_f32_16x16x32_f16 v[132:135], v[20:23], v[14:17], v[132:135]
	s_waitcnt lgkmcnt(0)
	v_mfma_f32_16x16x32_f16 v[132:135], v[6:9], v[28:31], v[132:135]
	s_nop 2
	v_mul_f32_e32 v96, 0x403504f3, v124
	v_mul_f32_e32 v97, 0x403504f3, v125
	v_mul_f32_e32 v98, 0x403504f3, v126
	v_mul_f32_e32 v99, 0x403504f3, v127
	v_cvt_pk_fp8_f32 v100, v96, v97
	v_cvt_pk_fp8_f32 v100, v98, v99 op_sel:[0,0,1]
	v_mul_f32_e32 v96, 4.0, v128
	v_mul_f32_e32 v97, 4.0, v129
	v_mul_f32_e32 v98, 4.0, v130
	v_mul_f32_e32 v99, 4.0, v131
	v_cvt_pk_fp8_f32 v101, v96, v97
	v_cvt_pk_fp8_f32 v101, v98, v99 op_sel:[0,0,1]
	global_store_dword v140, v100, s[32:33]
	global_store_dword v139, v101, s[32:33]
	v_mul_f32_e32 v96, 4.0, v132
	v_mul_f32_e32 v97, 4.0, v133
	v_mul_f32_e32 v98, 4.0, v134
	v_mul_f32_e32 v99, 4.0, v135
	v_cvt_pk_fp8_f32 v102, v96, v97
	v_cvt_pk_fp8_f32 v102, v98, v99 op_sel:[0,0,1]
	s_nop 0
	global_store_dword v122, v102, s[32:33]
	s_endpgm

	.amdhsa_kernel _Z11prep_kernelPKfS0_PKiS2_S0_S0_S0_S0_S0_S0_Pc
		.amdhsa_group_segment_fixed_size 13056
		.amdhsa_private_segment_fixed_size 0
		.amdhsa_kernarg_size 88
		.amdhsa_user_sgpr_count 2
		.amdhsa_user_sgpr_dispatch_ptr 0
		.amdhsa_user_sgpr_queue_ptr 0
		.amdhsa_user_sgpr_kernarg_segment_ptr 1
		.amdhsa_user_sgpr_dispatch_id 0
		.amdhsa_user_sgpr_kernarg_preload_length 0
		.amdhsa_user_sgpr_kernarg_preload_offset 0
		.amdhsa_user_sgpr_private_segment_size 0
		.amdhsa_uses_dynamic_stack 0
		.amdhsa_enable_private_segment 0
		.amdhsa_system_sgpr_workgroup_id_x 1
		.amdhsa_system_sgpr_workgroup_id_y 0
		.amdhsa_system_sgpr_workgroup_id_z 0
		.amdhsa_system_sgpr_workgroup_info 0
		.amdhsa_system_vgpr_workitem_id 0
		.amdhsa_next_free_vgpr 144
		.amdhsa_next_free_sgpr 91
		.amdhsa_accum_offset 144
		.amdhsa_reserve_vcc 1
		.amdhsa_float_round_mode_32 0
		.amdhsa_float_round_mode_16_64 0
		.amdhsa_float_denorm_mode_32 3
		.amdhsa_float_denorm_mode_16_64 3
		.amdhsa_dx10_clamp 1
		.amdhsa_ieee_mode 1
		.amdhsa_fp16_overflow 0
		.amdhsa_tg_split 0
		.amdhsa_exception_fp_ieee_invalid_op 0
		.amdhsa_exception_fp_denorm_src 0
		.amdhsa_exception_fp_ieee_div_zero 0
		.amdhsa_exception_fp_ieee_overflow 0
		.amdhsa_exception_fp_ieee_underflow 0
		.amdhsa_exception_fp_ieee_inexact 0
		.amdhsa_exception_int_div_zero 0
	.end_amdhsa_kernel

amdhsa.kernels:
  - .agpr_count:     0
    .args:
      - .actual_access:  read_only
        .address_space:  global
        .offset:         0
        .size:           8
        .value_kind:     global_buffer
      - .actual_access:  read_only
        .address_space:  global
        .offset:         8
        .size:           8
        .value_kind:     global_buffer
      - .actual_access:  read_only
        .address_space:  global
        .offset:         16
        .size:           8
        .value_kind:     global_buffer
      - .actual_access:  read_only
        .address_space:  global
        .offset:         24
        .size:           8
        .value_kind:     global_buffer
      - .actual_access:  read_only
        .address_space:  global
        .offset:         32
        .size:           8
        .value_kind:     global_buffer
      - .actual_access:  read_only
        .address_space:  global
        .offset:         40
        .size:           8
        .value_kind:     global_buffer
      - .actual_access:  read_only
        .address_space:  global
        .offset:         48
        .size:           8
        .value_kind:     global_buffer
      - .actual_access:  read_only
        .address_space:  global
        .offset:         56
        .size:           8
        .value_kind:     global_buffer
      - .actual_access:  read_only
        .address_space:  global
        .offset:         64
        .size:           8
        .value_kind:     global_buffer
      - .actual_access:  read_only
        .address_space:  global
        .offset:         72
        .size:           8
        .value_kind:     global_buffer
      - .actual_access:  write_only
        .address_space:  global
        .offset:         80
        .size:           8
        .value_kind:     global_buffer
    .group_segment_fixed_size: 13056
    .kernarg_segment_align: 8
    .kernarg_segment_size: 88
    .language:       OpenCL C
    .language_version:
      - 2
      - 0
    .max_flat_workgroup_size: 128
    .name:           _Z11prep_kernelPKfS0_PKiS2_S0_S0_S0_S0_S0_S0_Pc
    .private_segment_fixed_size: 0
    .sgpr_count:     38
    .sgpr_spill_count: 0
    .symbol:         _Z11prep_kernelPKfS0_PKiS2_S0_S0_S0_S0_S0_S0_Pc.kd
    .uniform_work_group_size: 1
    .uses_dynamic_stack: false
    .vgpr_count:     144
    .vgpr_spill_count: 0
    .wavefront_size: 64
  - .agpr_count:     0
    .args:
      - .actual_access:  read_only
        .address_space:  global
        .offset:         0
        .size:           8
        .value_kind:     global_buffer
      - .actual_access:  read_only
        .address_space:  global
        .offset:         8
        .size:           8
        .value_kind:     global_buffer
      - .actual_access:  read_only
        .address_space:  global
        .offset:         16
        .size:           8
        .value_kind:     global_buffer
      - .actual_access:  read_only
        .address_space:  global
        .offset:         24
        .size:           8
        .value_kind:     global_buffer
      - .actual_access:  read_only
        .address_space:  global
        .offset:         32
        .size:           8
        .value_kind:     global_buffer
      - .actual_access:  read_only
        .address_space:  global
        .offset:         40
        .size:           8
        .value_kind:     global_buffer
      - .actual_access:  read_only
        .address_space:  global
        .offset:         48
        .size:           8
        .value_kind:     global_buffer
      - .actual_access:  write_only
        .address_space:  global
        .offset:         56
        .size:           8
        .value_kind:     global_buffer
    .group_segment_fixed_size: 16640
    .kernarg_segment_align: 8
    .kernarg_segment_size: 64
    .language:       OpenCL C
    .language_version:
      - 2
      - 0
    .max_flat_workgroup_size: 256
    .name:           _Z11attn_kernelILi4EEvPKfS1_S1_S1_S1_S1_PKcPf
    .private_segment_fixed_size: 0
    .sgpr_count:     38
    .sgpr_spill_count: 0
    .symbol:         _Z11attn_kernelILi4EEvPKfS1_S1_S1_S1_S1_PKcPf.kd
    .uniform_work_group_size: 1
    .uses_dynamic_stack: false
    .vgpr_count:     250
    .vgpr_spill_count: 0
    .wavefront_size: 64
